# agg_ln1: per-node off4/cnt4 header via s_load_dwordx4 (scalar cache) instead of wave-uniform vector loads; type prefix sums in SALU
# baseline (speedup 1.0000x reference)
_Z7agg_ln1PKDF16_S0_S0_PKiS2_S2_PKfS4_S4_PDF16_S4_S4_S5_S5_:
	s_cmpk_gt_u32 s2, 0xff
	s_mov_b64 s[4:5], -1
	s_cbranch_scc0 .LBB1_28
	v_lshl_or_b32 v1, s2, 8, v0
	v_add_u32_e32 v1, 0xffff0000, v1
	s_mov_b32 s3, 0x9c400
	v_cmp_gt_u32_e32 vcc, s3, v1
	s_and_saveexec_b64 s[18:19], vcc
	s_cbranch_execz .LBB1_27
	s_load_dwordx2 s[4:5], s[0:1], 0x20
	s_load_dwordx2 s[6:7], s[0:1], 0x18
	s_load_dwordx2 s[32:33], s[0:1], 0x8
	v_lshrrev_b32_e32 v1, 6, v1
	v_lshlrev_b32_e32 v2, 4, v1
	v_and_b32_e32 v24, 63, v0
	v_lshlrev_b32_e32 v8, 3, v24
	v_lshlrev_b32_e32 v21, 10, v1
	v_lshl_add_u32 v21, v24, 4, v21
	s_waitcnt lgkmcnt(0)
	v_readfirstlane_b32 s34, v2
	global_load_dwordx4 v[60:63], v21, s[32:33] nt
	s_load_dwordx4 s[36:39], s[6:7], s34
	s_load_dwordx4 s[40:43], s[4:5], s34
	s_waitcnt lgkmcnt(0)
	s_add_u32 s34, s40, s41
	s_add_u32 s35, s34, s42
	s_add_u32 s35, s35, s43
	v_mov_b32_e32 v25, s35
	v_cmp_gt_i32_e32 vcc, 1, v25
	s_and_saveexec_b64 s[4:5], vcc
	s_xor_b64 s[4:5], exec, s[4:5]
	v_mov_b32_e32 v9, 0
	s_or_saveexec_b64 s[22:23], s[4:5]
	s_load_dwordx2 s[20:21], s[0:1], 0x48
	v_mov_b32_e32 v11, 0
	v_mov_b64_e32 v[18:19], 0
	v_mov_b32_e32 v10, v11
	v_mov_b32_e32 v13, v11
	v_mov_b32_e32 v12, v11
	v_mov_b32_e32 v15, v11
	v_mov_b32_e32 v14, v11
	v_mov_b32_e32 v17, v11
	v_mov_b32_e32 v16, v11
	s_xor_b64 exec, exec, s[22:23]
	s_cbranch_execz .LBB1_26
	s_load_dwordx2 s[24:25], s[0:1], 0x28
	s_load_dwordx2 s[26:27], s[0:1], 0x0
	s_mov_b32 s2, s35
	s_mov_b32 s4, s40
	s_mov_b32 s5, s34
	s_add_u32 s6, s34, s42
	s_mov_b32 s8, s36
	s_mov_b32 s9, s37
	s_mov_b32 s10, s38
	s_mov_b32 s11, s39
	v_lshrrev_b32_e32 v20, 3, v24
	v_lshlrev_b32_e32 v20, 2, v20
	v_mov_b32_e32 v9, 0
	v_mov_b32_e32 v10, 0
	v_mov_b32_e32 v11, 0
	v_mov_b32_e32 v12, 0
	v_mov_b32_e32 v13, 0
	v_mov_b32_e32 v14, 0
	v_mov_b32_e32 v15, 0
	v_mov_b32_e32 v16, 0
	v_mov_b32_e32 v17, 0
	s_sub_u32 s9, s9, s4
	s_sub_u32 s10, s10, s5
	s_sub_u32 s11, s11, s6
	s_mov_b64 s[12:13], 0
	s_mov_b32 s3, 0
	s_sub_u32 s7, s2, 1
	s_waitcnt lgkmcnt(0)
